# conversion reschedule: layer-0 hyena/idle slots convert layer-0 expert weights, displaced layer-1 items take the barrier-list tail, layer-1 hyena hosts 8192 items
# speedup vs baseline: 1.0118x; 1.0118x over previous
; __device__ __forceinline__ int f8w_bar_item(int wi, int i) {
;     if (i < F8W_BARQ0) return F8W_HOST0 - F8W_BARQ0 * F8W_BARW + wi + F8W_BARW * i;
;     return (wi < 896) ? (F8W_BAR0 + wi + 896 * (i - F8W_BARQ0)) : (F8W_BAR0 + 896 * (F8W_BARQ - 3) + (wi - 896) + 896 * (i - F8W_BARQ0)); }
; __device__ __forceinline__ void f8w_bar_flush(Frame& F, volatile LAS unsigned* st, int upto) {
;     ...
;     for (; i < upto; ++i) f8w_convert_one(F, f8w_bar_item(wi, i));
.LBB0_222:
	s_andn2_b64 vcc, exec, s[6:7]
	s_cbranch_vccnz .LBB0_224
	s_mul_i32 s2, s21, 0x700
	s_add_i32 s2, s12, s2
	s_cmp_ge_u32 s2, 0x5000
	s_cselect_b32 s6, 0x3400, 0
	s_add_i32 s2, s2, s6

; __device__ __forceinline__ void f8w_convert_idle(Frame& F) {
;     const int iw = ((int)blockIdx.x - 128) * NWAVES + F.wave;
;     for (int i = 0; i < F8W_IDLE; ++i) { const F8WItem it = f8w_item(F, F8W_HOST0 + F8W_HOSTED * 2048 + iw + 1024 * i); f32x4 v[16];
; __global__ void __launch_bounds__(NTHR, 2) fwd_kernel(Args args) {
;     ...
;     for (int l = 0; l < DEPTH; ++l) {
;         const int pb = 2 + l * PH_PER_LAYER;
;         const bool split = false, conv_role = false;
;         const int cidx = (int)blockIdx.x - NCOMP, ctot = (F8_NTILES - cidx + NCONV - 1) / NCONV, cq1 = 38, cq2 = 21;
.LBB0_280:
	s_cmpk_lt_i32 s88, 0x280
	s_cselect_b64 s[0:1], -1, 0
	s_ashr_i32 s2, s88, 31
	v_writelane_b32 v254, s2, 17
	s_lshr_b32 s2, s2, 29
	s_add_i32 s2, s88, s2
	s_ashr_i32 s8, s2, 3
	s_and_b32 s2, s2, -8
	s_sub_i32 s5, s88, s2
	s_cmpk_gt_i32 s88, 0x7f
	s_cselect_b64 s[2:3], -1, 0
	s_lshl_b32 s9, s88, 3
	v_writelane_b32 v254, s2, 18
	s_cmpk_lt_i32 s88, 0x100
	s_movk_i32 s4, 0x51
	v_writelane_b32 v254, s3, 19
	s_cselect_b64 s[2:3], -1, 0
	v_writelane_b32 v254, s2, 20
	v_cndmask_b32_e64 v1, 0, 1, s[0:1]
	s_movk_i32 s64, 0x2000
	v_writelane_b32 v254, s3, 21
	s_lshl_b32 s2, s5, 5
	s_cmp_lt_i32 s5, 0
	s_cselect_b32 s4, s4, 0x50
	s_mul_i32 s3, s5, 33
	s_mul_i32 s4, s5, s4
	v_writelane_b32 v254, s5, 22
	s_cselect_b32 s5, s3, s2
	s_add_i32 s4, s4, s8
	s_mul_hi_i32 s2, s4, 0x66666667
	s_lshr_b32 s3, s2, 31
	s_ashr_i32 s2, s2, 5
	s_add_i32 s2, s2, s3
	s_mul_i32 s3, s2, 0x50
	s_sub_i32 s3, s4, s3
	s_lshl_b32 s6, s2, 3
	s_bfe_i32 s2, s3, 0x80000
	s_bfe_u32 s2, s2, 0x3000c
	s_add_i32 s4, s3, s2
	s_bfe_i32 s2, s4, 0x80000
	s_and_b32 s4, s4, 0xf8
	s_sub_i32 s3, s3, s4
	s_sext_i32_i16 s7, s2
	s_sext_i32_i8 s3, s3
	s_lshr_b32 s2, s7, 3
	s_add_i32 s10, s6, s3
	s_ashr_i32 s3, s7, 3
	v_writelane_b32 v254, s3, 23
	s_bfe_i64 s[2:3], s[2:3], 0x100000
	s_lshl_b64 s[2:3], s[2:3], 19
	v_writelane_b32 v254, s2, 24
	s_add_i32 s0, 0, 0x20164
	s_ashr_i32 s11, s10, 31
	v_writelane_b32 v254, s3, 25
	s_add_i32 s2, s5, s8
	s_ashr_i32 s3, s2, 31
	s_lshr_b32 s3, s3, 27
	s_add_i32 s3, s2, s3
	s_ashr_i32 s4, s3, 5
	s_and_b32 s3, s3, 0xffe0
	s_sub_i32 s3, s2, s3
	s_bfe_i32 s2, s3, 0x80000
	s_bfe_u32 s2, s2, 0x3000c
	s_add_i32 s5, s3, s2
	s_bfe_i32 s2, s5, 0x80000
	s_and_b32 s5, s5, 0xf8
	s_sub_i32 s3, s3, s5
	s_lshl_b32 s4, s4, 3
	s_sext_i32_i16 s6, s2
	s_sext_i32_i8 s3, s3
	v_writelane_b32 v254, s8, 26
	s_lshr_b32 s2, s6, 3
	s_add_i32 s4, s4, s3
	s_ashr_i32 s3, s6, 3
	v_writelane_b32 v254, s3, 27
	s_bfe_i64 s[2:3], s[2:3], 0x100000
	s_lshl_b64 s[2:3], s[2:3], 19
	v_writelane_b32 v254, s2, 28
	s_ashr_i32 s5, s4, 31
	s_add_i32 s66, 0, 0x200d8
	v_writelane_b32 v254, s3, 29
	v_writelane_b32 v254, s9, 30
	s_add_i32 s2, s9, 0x4c00
	v_writelane_b32 v254, s2, 31
	s_add_i32 s70, 0, 0x20168
	v_readlane_b32 s2, v254, 14
	s_add_i32 s2, s2, 0x837f
	s_add_i32 s73, 0, 0x20040
	v_writelane_b32 v254, s2, 32
	s_lshl_b32 s2, s88, 6
	v_writelane_b32 v254, s2, 33
	v_writelane_b32 v254, s0, 34
	s_add_i32 s0, 0, 0x20058
	v_writelane_b32 v254, s0, 35
	s_add_i32 s0, 0, 0x20050
	v_writelane_b32 v254, s0, 36
	s_add_i32 s0, 0, 0x19100
	v_writelane_b32 v254, s0, 37
	s_add_i32 s0, 0, 0x10100
	v_writelane_b32 v254, s0, 38
	s_add_i32 s0, 0, 0x4040
	v_writelane_b32 v254, s0, 39
	s_add_i32 s0, 0, 0x8080
	v_writelane_b32 v254, s0, 40
	s_add_i32 s0, 0, 0xc0c0
	v_writelane_b32 v254, s0, 41
	s_add_i32 s0, 0, 0x200a0
	v_writelane_b32 v254, s0, 42
	s_add_i32 s0, 0, 0x20048
	v_writelane_b32 v254, s0, 43
	s_add_i32 s0, 0, 0x200c0
	v_writelane_b32 v254, s0, 44
	s_add_i32 s0, 0, 0x20028
	v_writelane_b32 v254, s0, 45
	s_add_i32 s0, 0, 0x200b0
	v_writelane_b32 v254, s0, 46
	s_add_i32 s0, 0, 0x200b8
	v_writelane_b32 v254, s0, 47
	s_add_i32 s0, 0, 0x20020
	v_writelane_b32 v254, s0, 48
	s_mov_b32 s0, s10
	v_writelane_b32 v254, s0, 49
	s_add_i32 s72, 0, 0x20060
	v_writelane_b32 v255, s73, 0
	v_writelane_b32 v254, s1, 50
	s_lshl_b64 s[0:1], s[10:11], 19
	v_writelane_b32 v254, s0, 51
	v_mov_b32_e32 v183, 0
	s_movk_i32 s62, 0x1400
	v_writelane_b32 v254, s1, 52
	s_mov_b32 s0, s4
	v_writelane_b32 v254, s0, 53
	s_movk_i32 s65, 0x90
	s_movk_i32 s67, 0xc8
	v_writelane_b32 v254, s1, 54
	s_lshl_b64 s[0:1], s[4:5], 19
	v_writelane_b32 v254, s0, 55
	s_movk_i32 s69, 0x1f00
	s_mov_b32 s33, 0xc3e00000
	v_writelane_b32 v254, s1, 56
	s_mov_b64 s[0:1], -1
	v_writelane_b32 v254, s0, 57
	v_mov_b32_e32 v224, 1
	s_mov_b32 s63, 0x800000
	v_writelane_b32 v254, s1, 58
	v_cmp_ne_u32_e64 s[0:1], 1, v1
	s_movk_i32 s71, 0x1000
	s_mov_b32 s74, 0xbfb8aa3b
	v_writelane_b32 v254, s0, 59
	s_mov_b32 s75, 0x3f317217
	s_mov_b32 s76, 0x7f800000
	v_writelane_b32 v254, s1, 60
	v_writelane_b32 v254, s66, 61
	v_writelane_b32 v254, s70, 62
	s_mov_b32 s77, 0x3d800000
	s_mov_b32 s78, 0x3fb8aa3b
	s_movk_i32 s79, 0x3f0
	v_mov_b32_e32 v225, 0x358637bd
	v_mov_b32_e32 v226, 0x43e00000
	v_mov_b32_e32 v227, 0x210
	v_mov_b32_e32 v228, 0x2c0000
	v_mov_b32_e32 v229, 0x580000
	v_not_b32_e32 v230, 63
	v_not_b32_e32 v231, 31
	v_mov_b32_e32 v232, 0x7fc00000
	v_mov_b32_e32 v233, 0x41b17218
	v_mov_b32_e32 v245, 0x3340
	v_mov_b32_e32 v236, 0x100
	v_mov_b32_e32 v237, 0x1400
	v_mov_b32_e32 v238, 0x600
	v_mov_b32_e32 v239, 0x400
	v_mov_b32_e32 v240, 0x200
	v_mov_b32_e32 v241, 0x9000
	v_mov_b32_e32 v242, 0x7f800000
	v_mov_b64_e32 v[184:185], 0x1ff
	s_movk_i32 s68, 0x1fff
	s_mov_b32 s92, 0x41000000
	s_mov_b32 s54, 0
	s_mov_b32 s95, 0
	s_mov_b64 s[6:7], 0
	s_mov_b64 s[90:91], 0x80
	s_mov_b64 s[96:97], 0x200000
	v_writelane_b32 v254, s72, 63
	v_writelane_b32 v255, s88, 1
	s_branch .LBB0_287

; #define LAS __attribute__((address_space(3)))
; __device__ __forceinline__ void f8w_bar_flush(Frame& F, volatile LAS unsigned* st, int upto) {
;     if (F.wave == 0) return;
;     const int wv = F.wave, wi = (int)blockIdx.x * 7 + wv - 1; int i = (int)st[8 + wv];
;     if (upto > F8W_BARQ0) upto = f8w_bar_count(wi);
;     if (i >= upto) return;
;     for (; i < upto; ++i) f8w_convert_one(F, f8w_bar_item(wi, i));
;     if (F.lane == 0) st[8 + wv] = (unsigned)upto;
; }
; __global__ void __launch_bounds__(NTHR, 2) fwd_kernel(Args args) {
;     ...
;             if (l == 1 && hostbar && (int)blockIdx.x >= 128) f8w_bar_flush(F, bar.st, F8W_BARQ0 + F8W_BARQ);
.LBB0_311:
	v_readlane_b32 s2, v254, 18
	v_readlane_b32 s3, v254, 19
	s_and_b64 s[2:3], s[2:3], s[6:7]
	s_cmp_gt_u32 s26, 63
	s_cselect_b64 s[4:5], -1, 0
	s_and_b64 s[2:3], s[2:3], s[4:5]
	v_and_b32_e32 v186, 63, v1
	s_andn2_b64 vcc, exec, s[2:3]
	s_cbranch_vccnz .LBB0_328
	s_lshl_b32 s2, s89, 2
	s_add_i32 s6, s2, 0
	s_add_i32 s6, s6, 0x20160
	v_mov_b32_e32 v2, s6
	ds_read_b32 v2, v2 offset:32
	v_readlane_b32 s2, v254, 14
	s_add_i32 s10, s89, s2
	s_cmpk_gt_i32 s10, 0x380
	s_cselect_b32 s7, 23, 20
	s_min_i32 s7, s7, 16
	s_waitcnt lgkmcnt(0)
	v_cmp_le_i32_e32 vcc, s7, v2
	v_readfirstlane_b32 s8, v2
	s_cbranch_vccnz .LBB0_328
	s_cmpk_gt_i32 s10, 0x380
	s_cselect_b64 s[2:3], -1, 0
	s_add_i32 s9, s10, 0x9bff
	s_addk_i32 s10, 0x1aff
	s_add_u32 s11, s58, 0x41400000
	s_addc_u32 s12, s59, 0
	s_add_u32 s13, s58, 0x2b400000
	v_readlane_b32 s4, v254, 32
	v_lshlrev_b32_e32 v2, 2, v1
	v_and_b32_e32 v1, 48, v1
	s_addc_u32 s14, s59, 0
	s_add_i32 s4, s4, s89
	s_mul_i32 s5, s8, 0x380
	v_and_b32_e32 v72, 60, v2
	v_lshlrev_b32_e32 v73, 12, v1
	s_add_i32 s15, s4, s5
	s_branch .LBB0_315

; __device__ __forceinline__ int f8w_bar_item(int wi, int i) {
;     if (i < F8W_BARQ0) return F8W_HOST0 - F8W_BARQ0 * F8W_BARW + wi + F8W_BARW * i;
;     return (wi < 896) ? (F8W_BAR0 + wi + 896 * (i - F8W_BARQ0)) : (F8W_BAR0 + 896 * (F8W_BARQ - 3) + (wi - 896) + 896 * (i - F8W_BARQ0)); }
; __device__ __forceinline__ void f8w_bar_flush(Frame& F, volatile LAS unsigned* st, int upto) {
;     ...
;     for (; i < upto; ++i) f8w_convert_one(F, f8w_bar_item(wi, i));
.LBB0_319:
	s_andn2_b64 vcc, exec, s[4:5]
	s_cbranch_vccnz .LBB0_321
	s_mul_i32 s4, s8, 0x700
	s_add_i32 s16, s10, s4
	s_cmp_ge_u32 s16, 0x5000
	s_cselect_b32 s4, 0x3400, 0
	s_add_i32 s16, s16, s4

; __device__ __forceinline__ int f8w_bar_item(int wi, int i) {
;     if (i < F8W_BARQ0) return F8W_HOST0 - F8W_BARQ0 * F8W_BARW + wi + F8W_BARW * i;
;     return (wi < 896) ? (F8W_BAR0 + wi + 896 * (i - F8W_BARQ0)) : (F8W_BAR0 + 896 * (F8W_BARQ - 3) + (wi - 896) + 896 * (i - F8W_BARQ0)); }
; __device__ __forceinline__ void f8w_bar_flush(Frame& F, volatile LAS unsigned* st, int upto) {
;     ...
;     for (; i < upto; ++i) f8w_convert_one(F, f8w_bar_item(wi, i));
.LBB0_391:
	s_andn2_b64 vcc, exec, s[8:9]
	s_cbranch_vccnz .LBB0_393
	s_mul_i32 s8, s15, 0x700
	s_add_i32 s16, s14, s8
	s_cmp_ge_u32 s16, 0x5000
	s_cselect_b32 s8, 0x3400, 0
	s_add_i32 s16, s16, s8

; #define LAS __attribute__((address_space(3)))
; __device__ __forceinline__ void hy_conv_item(Frame& F, int l, int c) {
;     ...
;     const int r = lane & 31, h = lane >> 5, q = r & 3, nT = 8 * w + (r >> 2), nb = r & 3;
;     hy_f32x16 acc0, acc1;
; #pragma unroll
;     for (int i = 0; i < 16; ++i) { acc0[i] = 0.f; acc1[i] = 0.f; }
;     const int a_base = q * HYC_CST + 4096 + 8 * h - (r - q);
;     hy_bf16x8 c2, c3;
;     {   const LAS bf16* ap = G + (a_base - 64 * (8 * w - 63)); c2 = *(const LAS hy_bf16x8_a8*)(ap + 32); c3 = *(const LAS hy_bf16x8_a8*)(ap + 48); }
;     const bool host = (l == 0) && (F.G == 256) && (c == F.vcu);
;     const int hq0 = F8W_HOST0 + F.vcu * NWAVES + w; F8WItem hit; f32x4 hv[16]; int di = 0;
.LBB0_664:
	s_cmpk_lt_i32 s22, 0x100
	s_mov_b64 s[56:57], s[84:85]
	s_cselect_b64 s[10:11], -1, 0
	s_cmpk_gt_i32 s22, 0xff
	s_mov_b64 s[58:59], s[86:87]
	s_mov_b64 s[86:87], s[82:83]
	s_movk_i32 s62, 0x1400
	s_mov_b32 s63, 0x800000
	s_movk_i32 s71, 0x1000
	v_readlane_b32 s72, v254, 63
	v_readlane_b32 s73, v255, 0
	s_mov_b32 s74, 0xbfb8aa3b
	s_mov_b32 s75, 0x3f317217
	s_mov_b32 s76, 0x7f800000
	s_mov_b32 s77, 0x3d800000
	v_readlane_b32 s47, v254, 38
	s_movk_i32 s48, 0x5ff
	s_movk_i32 s49, 0xe0f
	s_mov_b64 s[52:53], 0x8000
	s_mov_b64 s[54:55], 0x10000
	s_mov_b64 s[60:61], 0x18000
	s_cbranch_scc1 .LBB0_711
	s_add_u32 s24, s58, 0x600000
	v_readlane_b32 s2, v255, 5
	s_addc_u32 s25, s59, 0
	s_lshl_b32 s26, s2, 8
	s_movk_i32 s2, 0x800
	v_cmp_gt_i32_e64 s[4:5], s2, v1
	s_movk_i32 s2, 0x1010
	v_and_b32_e32 v144, 3, v1
	v_cmp_gt_i32_e64 s[6:7], s2, v1
	s_add_u32 s27, s58, 0xec00000
	v_lshlrev_b32_e32 v142, 2, v1
	v_readlane_b32 s2, v254, 37
	v_lshrrev_b32_e32 v4, 5, v186
	v_mul_u32_u24_e32 v5, 0x2020, v144
	s_waitcnt vmcnt(0)
	v_and_b32_e32 v6, 28, v1
	s_addc_u32 s28, s59, 0
	v_add_u32_e32 v143, s2, v142
	v_bfe_u32 v3, v1, 2, 3
	s_lshl_b32 s29, s89, 3
	v_lshlrev_b32_e32 v2, 3, v4
	v_sub_u32_e32 v5, v5, v6
	s_lshl_b32 s2, s89, 9
	v_or_b32_e32 v145, s29, v3
	v_add_u32_e32 v146, v5, v2
	s_addk_i32 s2, 0xf040
	v_lshl_add_u32 v151, v4, 4, s47
	v_mov_b32_e32 v4, 0x8dc0
	v_add_u32_e32 v147, 0x1000, v146
	v_subrev_u32_e32 v5, s2, v146
	s_cmpk_eq_i32 s23, 0x100
	v_readlane_b32 s12, v254, 57
	v_mad_u32_u24 v4, v144, s65, v4
	v_cmp_eq_u32_e32 vcc, 0, v3
	v_lshlrev_b32_e32 v182, 13, v144
	v_lshlrev_b32_e32 v6, 6, v145
	v_subrev_u32_e32 v148, s2, v147
	v_lshl_add_u32 v149, v5, 1, 0
	s_cselect_b64 s[2:3], -1, 0
	v_readlane_b32 s13, v254, 58
	v_cndmask_b32_e32 v152, v241, v4, vcc
	v_lshl_add_u64 v[4:5], s[58:59], 0, v[182:183]
	v_ashrrev_i32_e32 v7, 31, v6
	s_mov_b32 s100, s12
	s_mov_b64 s[12:13], s[2:3]
	s_or_b32 s30, s29, 7
	s_bfe_u32 s31, s31, 0x20006
	s_lshl_b32 s14, s22, 3
	v_lshl_add_u64 v[4:5], v[6:7], 1, v[4:5]
	v_mov_b32_e32 v3, v183
	s_add_u32 s34, s58, 0x41400000
	v_lshl_add_u64 v[2:3], v[4:5], 0, v[2:3]
	s_mov_b64 s[2:3], 0xf400000
	s_addc_u32 s35, s59, 0
	v_lshl_add_u64 v[138:139], v[2:3], 0, s[2:3]
	v_readlane_b32 s2, v254, 39
	v_and_b32_e32 v153, 60, v142
	s_add_u32 s36, s58, 0x2b400000
	v_lshlrev_b32_e32 v163, 3, v1
	v_add_u32_e32 v165, s2, v142
	v_readlane_b32 s2, v254, 40
	v_lshl_or_b32 v154, s31, 6, v153
	v_and_b32_e32 v155, 48, v1
	s_addc_u32 s37, s59, 0
	v_lshlrev_b32_e32 v159, 4, v1
	v_lshlrev_b32_e32 v162, 1, v1
	v_sub_u32_e32 v2, 0, v163
	v_add_u32_e32 v168, s2, v142
	v_readlane_b32 s2, v254, 41
	s_add_i32 s38, s89, s14
	v_cmp_gt_i32_e64 s[8:9], 36, v1
	v_add_u32_e32 v150, 0x2000, v149
	v_lshlrev_b32_e32 v156, 12, v155
	v_lshl_or_b32 v157, v154, 6, v155
	v_add_u32_e32 v158, 0xfffffe00, v1
	v_add_u32_e32 v160, s47, v159
	v_add_u32_e32 v161, 0, v142
	v_add_u32_e32 v164, 0x18100, v2
	v_add_u32_e32 v166, -1, v162
	v_add_u32_e32 v167, 0x18104, v2
	v_add_u32_e32 v169, -3, v162
	v_add_u32_e32 v170, 0x18108, v2
	v_add_u32_e32 v171, s2, v142
	v_add_u32_e32 v172, -4, v162
	v_add_u32_e32 v173, 0x1810c, v2
	s_and_b32 s101, s100, 0x6400
	s_add_i32 s38, s38, s101
	s_mov_b32 s14, s22
	s_branch .LBB0_667

; #define LAS __attribute__((address_space(3)))
; __device__ __forceinline__ void f8w_bar_flush(Frame& F, volatile LAS unsigned* st, int upto) {
;     if (F.wave == 0) return;
;     const int wv = F.wave, wi = (int)blockIdx.x * 7 + wv - 1; int i = (int)st[8 + wv];
;     if (upto > F8W_BARQ0) upto = f8w_bar_count(wi);
;     if (i >= upto) return;
;     for (; i < upto; ++i) f8w_convert_one(F, f8w_bar_item(wi, i));
;     if (F.lane == 0) st[8 + wv] = (unsigned)upto;
; __global__ void __launch_bounds__(NTHR, 2) fwd_kernel(Args args) {
;     ...
;         if (hostbar) { frame_fence(F); f8w_bar_flush(F, bar.st, l == 0 ? F8W_BARQ0 : F8W_BARQ0 + F8W_BARQ); }
.LBB0_1507:
	v_readlane_b32 s0, v254, 12
	v_readlane_b32 s1, v254, 13
	s_andn2_b64 vcc, exec, s[0:1]
	s_cbranch_vccnz .LBB0_1525
	v_readlane_b32 s0, v254, 8
	v_readlane_b32 s1, v254, 9
	v_mov_b32_e32 v2, v0
	v_writelane_b32 v254, s0, 8
	s_nop 1
	v_writelane_b32 v254, s1, 9
	s_movk_i32 s0, 0x100
	s_nop 0
	v_readfirstlane_b32 s0, v2
	s_ashr_i32 s89, s0, 6
	s_cmp_lt_u32 s0, 64
	v_and_b32_e32 v186, 63, v2
	s_cbranch_scc1 .LBB0_1525
	v_readlane_b32 s0, v254, 14
	s_add_i32 s8, s89, s0
	s_lshl_b32 s0, s89, 2
	s_add_i32 s4, s0, 0
	s_add_i32 s4, s4, 0x20160
	v_mov_b32_e32 v1, s4
	ds_read_b32 v1, v1 offset:32
	v_readlane_b32 s0, v254, 57
	s_cmpk_gt_i32 s8, 0x380
	v_readlane_b32 s1, v254, 58
	s_cselect_b32 s2, 23, 20
	s_cmpk_gt_i32 s8, 0x400
	s_cselect_b32 s5, 7, 8
	s_and_b64 s[0:1], s[0:1], exec
	s_cselect_b32 s5, s5, s2
	s_waitcnt lgkmcnt(0)
	v_cmp_le_i32_e32 vcc, s5, v1
	v_readfirstlane_b32 s6, v1
	s_cbranch_vccnz .LBB0_1525
	s_cmpk_gt_i32 s8, 0x380
	s_cselect_b64 s[0:1], -1, 0
	s_add_i32 s7, s8, 0x9bff
	s_addk_i32 s8, 0x1aff
	s_add_u32 s9, s80, 0x41400000
	s_addc_u32 s10, s81, 0
	s_add_u32 s11, s80, 0x2b400000
	v_readlane_b32 s2, v254, 32
	v_lshlrev_b32_e32 v1, 2, v2
	v_and_b32_e32 v72, 48, v2
	s_addc_u32 s12, s81, 0
	s_add_i32 s2, s2, s89
	s_mul_i32 s3, s6, 0x380
	v_and_b32_e32 v1, 60, v1
	v_lshlrev_b32_e32 v73, 12, v72
	s_add_i32 s13, s2, s3
	s_branch .LBB0_1512

; __device__ __forceinline__ int f8w_bar_item(int wi, int i) {
;     if (i < F8W_BARQ0) return F8W_HOST0 - F8W_BARQ0 * F8W_BARW + wi + F8W_BARW * i;
;     return (wi < 896) ? (F8W_BAR0 + wi + 896 * (i - F8W_BARQ0)) : (F8W_BAR0 + 896 * (F8W_BARQ - 3) + (wi - 896) + 896 * (i - F8W_BARQ0)); }
; __device__ __forceinline__ void f8w_bar_flush(Frame& F, volatile LAS unsigned* st, int upto) {
;     ...
;     for (; i < upto; ++i) f8w_convert_one(F, f8w_bar_item(wi, i));
.LBB0_1516:
	s_andn2_b64 vcc, exec, s[2:3]
	s_cbranch_vccnz .LBB0_1518
	s_mul_i32 s2, s6, 0x700
	s_add_i32 s14, s8, s2
	s_cmp_ge_u32 s14, 0x5000
	s_cselect_b32 s2, 0x3400, 0
	s_add_i32 s14, s14, s2
